# v35_frag
# speedup vs baseline: 1.0131x; 1.0131x over previous
.LBB3_12:
	s_or_b64 exec, exec, s[20:21]
	v_mov_b32_e32 v107, v67
	ds_write_b128 v123, v[22:25] offset:35776
	ds_write_b128 v124, v[26:29] offset:40896
	ds_write_b128 v125, v[30:33] offset:46016
	ds_write_b128 v126, v[34:37] offset:51136
	ds_write_b128 v127, v[38:41] offset:56256
	v_lshl_add_u64 v[22:23], s[56:57], 0, v[106:107]
	v_add_co_u32_e32 v24, vcc, 0xc000, v22
	s_waitcnt lgkmcnt(0)
	s_nop 0
	v_addc_co_u32_e32 v25, vcc, 0, v23, vcc
	v_add_co_u32_e32 v28, vcc, 0xd000, v22
	s_barrier
	v_add_u32_e32 v196, 0x6f80, v129
	v_add_u32_e32 v197, 0x6f80, v123
	v_add_u32_e32 v198, 0x6f80, v124
	v_add_u32_e32 v199, 0x6f80, v125
	v_add_u32_e32 v200, 0x6f80, v126
	v_add_u32_e32 v201, 0x6f80, v127
	s_nop 0
	v_addc_co_u32_e32 v29, vcc, 0, v23, vcc
	v_add_co_u32_e32 v32, vcc, 0xf000, v22
	s_nop 1
	v_addc_co_u32_e32 v33, vcc, 0, v23, vcc
	v_add_co_u32_e32 v36, vcc, 0x10000, v22
	global_load_dwordx4 v[24:27], v[24:25], off offset:2048
	s_nop 0
	global_load_dwordx4 v[28:31], v[28:29], off offset:3072
	v_addc_co_u32_e32 v37, vcc, 0, v23, vcc
	v_add_co_u32_e32 v40, vcc, 0x11000, v22
	global_load_dwordx4 v[32:35], v[32:33], off
	s_nop 0
	global_load_dwordx4 v[36:39], v[36:37], off offset:1024
	v_addc_co_u32_e32 v41, vcc, 0, v23, vcc
	global_load_dwordx4 v[40:43], v[40:41], off offset:2048
	ds_write_b128 v197, v[2:5] offset:35776
	ds_write_b128 v198, v[6:9] offset:40896
	ds_write_b128 v199, v[10:13] offset:46016
	ds_write_b128 v200, v[14:17] offset:51136
	ds_write_b128 v201, v[18:21] offset:56256
	s_waitcnt vmcnt(5)
	ds_read_b128 v[44:47], v129 offset:35776
	ds_read_b128 v[48:51], v144
	ds_read_b128 v[52:55], v144 offset:64
	ds_read_b128 v[56:59], v129 offset:35840
	ds_read_b128 v[60:63], v129 offset:42432
	ds_read_b128 v[152:155], v129 offset:42496
	ds_read_b128 v[156:159], v129 offset:49088
	ds_read_b128 v[160:163], v129 offset:49152
	s_waitcnt lgkmcnt(6)
	v_mfma_f32_16x16x32_f16 v[44:47], v[44:47], v[48:51], 0
	ds_read_b128 v[164:167], v129 offset:55744
	ds_read_b128 v[168:171], v129 offset:55808
	s_waitcnt lgkmcnt(5)
	v_mfma_f32_16x16x32_f16 v[60:63], v[60:63], v[48:51], 0
	v_mfma_f32_16x16x32_f16 v[44:47], v[56:59], v[52:55], v[44:47]
	s_waitcnt lgkmcnt(4)
	v_mfma_f32_16x16x32_f16 v[56:59], v[152:155], v[52:55], v[60:63]
	ds_read_b128 v[152:155], v129 offset:35904
	s_waitcnt lgkmcnt(4)
	v_mfma_f32_16x16x32_f16 v[156:159], v[156:159], v[48:51], 0
	s_waitcnt lgkmcnt(2)
	v_mfma_f32_16x16x32_f16 v[48:51], v[164:167], v[48:51], 0
	v_mfma_f32_16x16x32_f16 v[60:63], v[160:163], v[52:55], v[156:159]
	s_waitcnt lgkmcnt(1)
	v_mfma_f32_16x16x32_f16 v[48:51], v[168:171], v[52:55], v[48:51]
	ds_read_b128 v[52:55], v144 offset:128
	s_nop 1
	ds_read_b128 v[156:159], v144 offset:192
	ds_read_b128 v[160:163], v129 offset:35968
	s_waitcnt lgkmcnt(2)
	v_mfma_f32_16x16x32_f16 v[44:47], v[152:155], v[52:55], v[44:47]
	ds_read_b128 v[152:155], v129 offset:42560
	ds_read_b128 v[164:167], v129 offset:42624
	s_waitcnt lgkmcnt(1)
	v_mfma_f32_16x16x32_f16 v[56:59], v[152:155], v[52:55], v[56:59]
	ds_read_b128 v[152:155], v129 offset:49216
	ds_read_b128 v[168:171], v129 offset:49280
	s_waitcnt lgkmcnt(1)
	v_mfma_f32_16x16x32_f16 v[60:63], v[152:155], v[52:55], v[60:63]
	ds_read_b128 v[152:155], v129 offset:55872
	ds_read_b128 v[172:175], v129 offset:55936
	s_waitcnt lgkmcnt(1)
	v_mfma_f32_16x16x32_f16 v[48:51], v[152:155], v[52:55], v[48:51]
	v_mfma_f32_16x16x32_f16 v[44:47], v[160:163], v[156:159], v[44:47]
	ds_read_b128 v[52:55], v144 offset:256
	ds_read_b128 v[152:155], v144 offset:320
	ds_read_b128 v[160:163], v129 offset:36032
	ds_read_b128 v[176:179], v129 offset:36096
	v_mfma_f32_16x16x32_f16 v[56:59], v[164:167], v[156:159], v[56:59]
	ds_read_b128 v[164:167], v129 offset:42688
	ds_read_b128 v[180:183], v129 offset:42752
	ds_read_b128 v[184:187], v129 offset:49344
	ds_read_b128 v[188:191], v129 offset:49408
	v_mfma_f32_16x16x32_f16 v[60:63], v[168:171], v[156:159], v[60:63]
	ds_read_b128 v[168:171], v129 offset:56000
	ds_read_b128 v[192:195], v129 offset:56064
	s_waitcnt lgkmcnt(0)
	v_mfma_f32_16x16x32_f16 v[48:51], v[172:175], v[156:159], v[48:51]
	v_add_co_u32_e32 v18, vcc, s75, v22
	v_mfma_f32_16x16x32_f16 v[2:5], v[160:163], v[52:55], v[44:47]
	s_nop 0
	v_addc_co_u32_e32 v19, vcc, 0, v23, vcc
	s_waitcnt lgkmcnt(0)
	v_add_co_u32_e32 v44, vcc, s76, v22
	v_mfma_f32_16x16x32_f16 v[14:17], v[168:171], v[52:55], v[48:51]
	s_nop 0
	v_addc_co_u32_e32 v45, vcc, 0, v23, vcc
	s_barrier
	v_add_co_u32_e32 v48, vcc, s77, v22
	v_mfma_f32_16x16x32_f16 v[6:9], v[164:167], v[52:55], v[56:59]
	s_nop 0
	v_addc_co_u32_e32 v49, vcc, 0, v23, vcc
	v_mfma_f32_16x16x32_f16 v[10:13], v[184:187], v[52:55], v[60:63]
	v_add_co_u32_e32 v52, vcc, s78, v22
	global_load_dwordx4 v[18:21], v[18:19], off offset:3072
	s_nop 0
	global_load_dwordx4 v[44:47], v[44:45], off
	v_addc_co_u32_e32 v53, vcc, 0, v23, vcc
	v_add_co_u32_e32 v56, vcc, s79, v22
	global_load_dwordx4 v[48:51], v[48:49], off offset:1024
	s_nop 0
	global_load_dwordx4 v[52:55], v[52:53], off offset:2048
	v_addc_co_u32_e32 v57, vcc, 0, v23, vcc
	global_load_dwordx4 v[56:59], v[56:57], off offset:3072
	s_waitcnt vmcnt(9)
	ds_write_b128 v123, v[24:27] offset:35776
	s_waitcnt vmcnt(8)
	ds_write_b128 v124, v[28:31] offset:40896
	s_waitcnt vmcnt(7)
	ds_write_b128 v125, v[32:35] offset:46016
	s_waitcnt vmcnt(6)
	ds_write_b128 v126, v[36:39] offset:51136
	s_waitcnt vmcnt(5)
	ds_write_b128 v127, v[40:43] offset:56256
	v_mfma_f32_16x16x32_f16 v[2:5], v[176:179], v[152:155], v[2:5]
	v_mfma_f32_16x16x32_f16 v[6:9], v[180:183], v[152:155], v[6:9]
	v_mfma_f32_16x16x32_f16 v[10:13], v[188:191], v[152:155], v[10:13]
	v_mfma_f32_16x16x32_f16 v[14:17], v[192:195], v[152:155], v[14:17]
	ds_read_b128 v[60:63], v196 offset:35776
	ds_read_b128 v[152:155], v144 offset:416
	ds_read_b128 v[208:211], v196 offset:42432
	ds_read_b128 v[212:215], v196 offset:49088
	ds_read_b128 v[216:219], v196 offset:55744
	ds_read_b128 v[156:159], v144 offset:480
	ds_read_b128 v[160:163], v196 offset:35840
	ds_read_b128 v[164:167], v196 offset:42496
	ds_read_b128 v[168:171], v196 offset:49152
	ds_read_b128 v[172:175], v196 offset:55808
	s_waitcnt lgkmcnt(8)
	v_mfma_f32_16x16x32_f16 v[2:5], v[60:63], v[152:155], v[2:5]
	s_waitcnt lgkmcnt(7)
	v_mfma_f32_16x16x32_f16 v[6:9], v[208:211], v[152:155], v[6:9]
	s_waitcnt lgkmcnt(6)
	v_mfma_f32_16x16x32_f16 v[10:13], v[212:215], v[152:155], v[10:13]
	s_waitcnt lgkmcnt(5)
	v_mfma_f32_16x16x32_f16 v[14:17], v[216:219], v[152:155], v[14:17]
	s_waitcnt lgkmcnt(0)
	ds_read_b128 v[60:63], v196 offset:35904
	v_mfma_f32_16x16x32_f16 v[2:5], v[160:163], v[156:159], v[2:5]
	v_mfma_f32_16x16x32_f16 v[6:9], v[164:167], v[156:159], v[6:9]
	v_mfma_f32_16x16x32_f16 v[10:13], v[168:171], v[156:159], v[10:13]
	s_waitcnt lgkmcnt(1)
	v_mfma_f32_16x16x32_f16 v[14:17], v[172:175], v[156:159], v[14:17]
	ds_read_b128 v[152:155], v144 offset:544
	ds_read_b128 v[208:211], v196 offset:42560
	ds_read_b128 v[212:215], v196 offset:49216
	ds_read_b128 v[216:219], v196 offset:55872
	ds_read_b128 v[156:159], v144 offset:608
	ds_read_b128 v[160:163], v196 offset:35968
	ds_read_b128 v[164:167], v196 offset:42624
	ds_read_b128 v[168:171], v196 offset:49280
	ds_read_b128 v[172:175], v196 offset:55936
	s_waitcnt lgkmcnt(8)
	v_mfma_f32_16x16x32_f16 v[2:5], v[60:63], v[152:155], v[2:5]
	s_waitcnt lgkmcnt(7)
	v_mfma_f32_16x16x32_f16 v[6:9], v[208:211], v[152:155], v[6:9]
	s_waitcnt lgkmcnt(6)
	v_mfma_f32_16x16x32_f16 v[10:13], v[212:215], v[152:155], v[10:13]
	s_waitcnt lgkmcnt(5)
	v_mfma_f32_16x16x32_f16 v[14:17], v[216:219], v[152:155], v[14:17]
	s_waitcnt lgkmcnt(0)
	v_mfma_f32_16x16x32_f16 v[2:5], v[160:163], v[156:159], v[2:5]
	ds_read_b128 v[60:63], v144 offset:672
	ds_read_b128 v[152:155], v144 offset:736
	ds_read_b128 v[160:163], v196 offset:36032
	ds_read_b128 v[176:179], v196 offset:36096
	v_mfma_f32_16x16x32_f16 v[6:9], v[164:167], v[156:159], v[6:9]
	ds_read_b128 v[164:167], v196 offset:42688
	ds_read_b128 v[180:183], v196 offset:42752
	ds_read_b128 v[184:187], v196 offset:49344
	ds_read_b128 v[188:191], v196 offset:49408
	v_mfma_f32_16x16x32_f16 v[10:13], v[168:171], v[156:159], v[10:13]
	ds_read_b128 v[168:171], v196 offset:56000
	ds_read_b128 v[192:195], v196 offset:56064
	s_waitcnt lgkmcnt(0)
	v_add_co_u32_e32 v24, vcc, s80, v22
	v_addc_co_u32_e32 v25, vcc, 0, v23, vcc
	v_add_co_u32_e32 v28, vcc, s81, v22
	s_waitcnt lgkmcnt(0)
	s_nop 0
	v_addc_co_u32_e32 v29, vcc, 0, v23, vcc
	v_add_co_u32_e32 v32, vcc, s82, v22
	s_barrier
	s_nop 0
	v_addc_co_u32_e32 v33, vcc, 0, v23, vcc
	v_add_co_u32_e32 v36, vcc, s83, v22
	s_nop 1
	v_addc_co_u32_e32 v37, vcc, 0, v23, vcc
	v_add_co_u32_e32 v40, vcc, s84, v22
	global_load_dwordx4 v[24:27], v[24:25], off
	s_nop 0
	global_load_dwordx4 v[28:31], v[28:29], off offset:1024
	s_nop 0
	global_load_dwordx4 v[32:35], v[32:33], off offset:2048
	s_nop 0
	global_load_dwordx4 v[36:39], v[36:37], off offset:3072
	v_addc_co_u32_e32 v41, vcc, 0, v23, vcc
	global_load_dwordx4 v[40:43], v[40:41], off
	s_waitcnt vmcnt(9)
	ds_write_b128 v197, v[18:21] offset:35776
	s_waitcnt vmcnt(8)
	ds_write_b128 v198, v[44:47] offset:40896
	s_waitcnt vmcnt(7)
	ds_write_b128 v199, v[48:51] offset:46016
	s_waitcnt vmcnt(6)
	ds_write_b128 v200, v[52:55] offset:51136
	s_waitcnt vmcnt(5)
	ds_write_b128 v201, v[56:59] offset:56256
	v_mfma_f32_16x16x32_f16 v[14:17], v[172:175], v[156:159], v[14:17]
	v_mfma_f32_16x16x32_f16 v[2:5], v[160:163], v[60:63], v[2:5]
	v_mfma_f32_16x16x32_f16 v[6:9], v[164:167], v[60:63], v[6:9]
	v_mfma_f32_16x16x32_f16 v[10:13], v[184:187], v[60:63], v[10:13]
	v_mfma_f32_16x16x32_f16 v[14:17], v[168:171], v[60:63], v[14:17]
	v_mfma_f32_16x16x32_f16 v[2:5], v[176:179], v[152:155], v[2:5]
	v_mfma_f32_16x16x32_f16 v[6:9], v[180:183], v[152:155], v[6:9]
	v_mfma_f32_16x16x32_f16 v[10:13], v[188:191], v[152:155], v[10:13]
	v_mfma_f32_16x16x32_f16 v[14:17], v[192:195], v[152:155], v[14:17]
	ds_read_b128 v[60:63], v129 offset:35776
	ds_read_b128 v[152:155], v144 offset:832
	ds_read_b128 v[208:211], v129 offset:42432
	ds_read_b128 v[212:215], v129 offset:49088
	ds_read_b128 v[216:219], v129 offset:55744
	ds_read_b128 v[156:159], v144 offset:896
	ds_read_b128 v[160:163], v129 offset:35840
	ds_read_b128 v[164:167], v129 offset:42496
	ds_read_b128 v[168:171], v129 offset:49152
	ds_read_b128 v[172:175], v129 offset:55808
	s_waitcnt lgkmcnt(8)
	v_mfma_f32_16x16x32_f16 v[2:5], v[60:63], v[152:155], v[2:5]
	s_waitcnt lgkmcnt(7)
	v_mfma_f32_16x16x32_f16 v[6:9], v[208:211], v[152:155], v[6:9]
	s_waitcnt lgkmcnt(6)
	v_mfma_f32_16x16x32_f16 v[10:13], v[212:215], v[152:155], v[10:13]
	s_waitcnt lgkmcnt(5)
	v_mfma_f32_16x16x32_f16 v[14:17], v[216:219], v[152:155], v[14:17]
	s_waitcnt lgkmcnt(0)
	ds_read_b128 v[60:63], v129 offset:35904
	v_mfma_f32_16x16x32_f16 v[2:5], v[160:163], v[156:159], v[2:5]
	v_mfma_f32_16x16x32_f16 v[6:9], v[164:167], v[156:159], v[6:9]
	v_mfma_f32_16x16x32_f16 v[10:13], v[168:171], v[156:159], v[10:13]
	s_waitcnt lgkmcnt(1)
	v_mfma_f32_16x16x32_f16 v[14:17], v[172:175], v[156:159], v[14:17]
	ds_read_b128 v[152:155], v144 offset:960
	ds_read_b128 v[208:211], v129 offset:42560
	ds_read_b128 v[212:215], v129 offset:49216
	ds_read_b128 v[216:219], v129 offset:55872
	ds_read_b128 v[156:159], v144 offset:1024
	ds_read_b128 v[160:163], v129 offset:35968
	ds_read_b128 v[164:167], v129 offset:42624
	ds_read_b128 v[168:171], v129 offset:49280
	ds_read_b128 v[172:175], v129 offset:55936
	s_waitcnt lgkmcnt(8)
	v_mfma_f32_16x16x32_f16 v[2:5], v[60:63], v[152:155], v[2:5]
	s_waitcnt lgkmcnt(7)
	v_mfma_f32_16x16x32_f16 v[6:9], v[208:211], v[152:155], v[6:9]
	s_waitcnt lgkmcnt(6)
	v_mfma_f32_16x16x32_f16 v[10:13], v[212:215], v[152:155], v[10:13]
	s_waitcnt lgkmcnt(5)
	v_mfma_f32_16x16x32_f16 v[14:17], v[216:219], v[152:155], v[14:17]
	s_waitcnt lgkmcnt(0)
	v_mfma_f32_16x16x32_f16 v[2:5], v[160:163], v[156:159], v[2:5]
	ds_read_b128 v[60:63], v144 offset:1088
	ds_read_b128 v[152:155], v144 offset:1152
	ds_read_b128 v[160:163], v129 offset:36032
	ds_read_b128 v[176:179], v129 offset:36096
	v_mfma_f32_16x16x32_f16 v[6:9], v[164:167], v[156:159], v[6:9]
	ds_read_b128 v[164:167], v129 offset:42688
	ds_read_b128 v[180:183], v129 offset:42752
	ds_read_b128 v[184:187], v129 offset:49344
	ds_read_b128 v[188:191], v129 offset:49408
	v_mfma_f32_16x16x32_f16 v[10:13], v[168:171], v[156:159], v[10:13]
	ds_read_b128 v[168:171], v129 offset:56000
	ds_read_b128 v[192:195], v129 offset:56064
	s_waitcnt lgkmcnt(0)
	v_add_co_u32_e32 v18, vcc, s85, v22
	v_addc_co_u32_e32 v19, vcc, 0, v23, vcc
	v_add_co_u32_e32 v44, vcc, s27, v22
	s_waitcnt lgkmcnt(0)
	s_nop 0
	v_addc_co_u32_e32 v45, vcc, 0, v23, vcc
	v_add_co_u32_e32 v48, vcc, s86, v22
	s_barrier
	s_nop 0
	v_addc_co_u32_e32 v49, vcc, 0, v23, vcc
	v_add_co_u32_e32 v52, vcc, s87, v22
	s_nop 1
	v_addc_co_u32_e32 v53, vcc, 0, v23, vcc
	v_add_co_u32_e32 v56, vcc, s88, v22
	global_load_dwordx4 v[18:21], v[18:19], off offset:1024
	s_nop 0
	global_load_dwordx4 v[44:47], v[44:45], off offset:2048
	s_nop 0
	global_load_dwordx4 v[48:51], v[48:49], off offset:3072
	s_nop 0
	global_load_dwordx4 v[52:55], v[52:53], off
	v_addc_co_u32_e32 v57, vcc, 0, v23, vcc
	global_load_dwordx4 v[56:59], v[56:57], off offset:1024
	s_waitcnt vmcnt(9)
	ds_write_b128 v123, v[24:27] offset:35776
	s_waitcnt vmcnt(8)
	ds_write_b128 v124, v[28:31] offset:40896
	s_waitcnt vmcnt(7)
	ds_write_b128 v125, v[32:35] offset:46016
	s_waitcnt vmcnt(6)
	ds_write_b128 v126, v[36:39] offset:51136
	s_waitcnt vmcnt(5)
	ds_write_b128 v127, v[40:43] offset:56256
	v_mfma_f32_16x16x32_f16 v[14:17], v[172:175], v[156:159], v[14:17]
	v_mfma_f32_16x16x32_f16 v[2:5], v[160:163], v[60:63], v[2:5]
	v_mfma_f32_16x16x32_f16 v[6:9], v[164:167], v[60:63], v[6:9]
	v_mfma_f32_16x16x32_f16 v[10:13], v[184:187], v[60:63], v[10:13]
	v_mfma_f32_16x16x32_f16 v[14:17], v[168:171], v[60:63], v[14:17]
	v_mfma_f32_16x16x32_f16 v[2:5], v[176:179], v[152:155], v[2:5]
	v_mfma_f32_16x16x32_f16 v[6:9], v[180:183], v[152:155], v[6:9]
	v_mfma_f32_16x16x32_f16 v[10:13], v[188:191], v[152:155], v[10:13]
	v_mfma_f32_16x16x32_f16 v[14:17], v[192:195], v[152:155], v[14:17]
	ds_read_b128 v[60:63], v196 offset:35776
	ds_read_b128 v[152:155], v144 offset:1248
	ds_read_b128 v[208:211], v196 offset:42432
	ds_read_b128 v[212:215], v196 offset:49088
	ds_read_b128 v[216:219], v196 offset:55744
	ds_read_b128 v[156:159], v144 offset:1312
	ds_read_b128 v[160:163], v196 offset:35840
	ds_read_b128 v[164:167], v196 offset:42496
	ds_read_b128 v[168:171], v196 offset:49152
	ds_read_b128 v[172:175], v196 offset:55808
	s_waitcnt lgkmcnt(8)
	v_mfma_f32_16x16x32_f16 v[2:5], v[60:63], v[152:155], v[2:5]
	s_waitcnt lgkmcnt(7)
	v_mfma_f32_16x16x32_f16 v[6:9], v[208:211], v[152:155], v[6:9]
	s_waitcnt lgkmcnt(6)
	v_mfma_f32_16x16x32_f16 v[10:13], v[212:215], v[152:155], v[10:13]
	s_waitcnt lgkmcnt(5)
	v_mfma_f32_16x16x32_f16 v[14:17], v[216:219], v[152:155], v[14:17]
	s_waitcnt lgkmcnt(0)
	ds_read_b128 v[60:63], v196 offset:35904
	v_mfma_f32_16x16x32_f16 v[2:5], v[160:163], v[156:159], v[2:5]
	v_mfma_f32_16x16x32_f16 v[6:9], v[164:167], v[156:159], v[6:9]
	v_mfma_f32_16x16x32_f16 v[10:13], v[168:171], v[156:159], v[10:13]
	s_waitcnt lgkmcnt(1)
	v_mfma_f32_16x16x32_f16 v[14:17], v[172:175], v[156:159], v[14:17]
	ds_read_b128 v[152:155], v144 offset:1376
	ds_read_b128 v[208:211], v196 offset:42560
	ds_read_b128 v[212:215], v196 offset:49216
	ds_read_b128 v[216:219], v196 offset:55872
	ds_read_b128 v[156:159], v144 offset:1440
	ds_read_b128 v[160:163], v196 offset:35968
	ds_read_b128 v[164:167], v196 offset:42624
	ds_read_b128 v[168:171], v196 offset:49280
	ds_read_b128 v[172:175], v196 offset:55936
	s_waitcnt lgkmcnt(8)
	v_mfma_f32_16x16x32_f16 v[2:5], v[60:63], v[152:155], v[2:5]
	s_waitcnt lgkmcnt(7)
	v_mfma_f32_16x16x32_f16 v[6:9], v[208:211], v[152:155], v[6:9]
	s_waitcnt lgkmcnt(6)
	v_mfma_f32_16x16x32_f16 v[10:13], v[212:215], v[152:155], v[10:13]
	s_waitcnt lgkmcnt(5)
	v_mfma_f32_16x16x32_f16 v[14:17], v[216:219], v[152:155], v[14:17]
	s_waitcnt lgkmcnt(0)
	v_mfma_f32_16x16x32_f16 v[2:5], v[160:163], v[156:159], v[2:5]
	ds_read_b128 v[60:63], v144 offset:1504
	ds_read_b128 v[152:155], v144 offset:1568
	ds_read_b128 v[160:163], v196 offset:36032
	ds_read_b128 v[176:179], v196 offset:36096
	v_mfma_f32_16x16x32_f16 v[6:9], v[164:167], v[156:159], v[6:9]
	ds_read_b128 v[164:167], v196 offset:42688
	ds_read_b128 v[180:183], v196 offset:42752
	ds_read_b128 v[184:187], v196 offset:49344
	ds_read_b128 v[188:191], v196 offset:49408
	v_mfma_f32_16x16x32_f16 v[10:13], v[168:171], v[156:159], v[10:13]
	ds_read_b128 v[168:171], v196 offset:56000
	ds_read_b128 v[192:195], v196 offset:56064
	s_waitcnt lgkmcnt(0)
	v_add_co_u32_e32 v24, vcc, s89, v22
	v_addc_co_u32_e32 v25, vcc, 0, v23, vcc
	v_add_co_u32_e32 v28, vcc, s90, v22
	s_waitcnt lgkmcnt(0)
	s_nop 0
	v_addc_co_u32_e32 v29, vcc, 0, v23, vcc
	v_add_co_u32_e32 v32, vcc, s91, v22
	s_barrier
	s_nop 0
	v_addc_co_u32_e32 v33, vcc, 0, v23, vcc
	v_add_co_u32_e32 v36, vcc, s92, v22
	s_nop 1
	v_addc_co_u32_e32 v37, vcc, 0, v23, vcc
	v_add_co_u32_e32 v22, vcc, s93, v22
	global_load_dwordx4 v[24:27], v[24:25], off offset:2048
	s_nop 0
	global_load_dwordx4 v[28:31], v[28:29], off offset:3072
	s_nop 0
	global_load_dwordx4 v[32:35], v[32:33], off
	s_nop 0
	global_load_dwordx4 v[36:39], v[36:37], off offset:1024
	v_addc_co_u32_e32 v23, vcc, 0, v23, vcc
	global_load_dwordx4 v[40:43], v[22:23], off offset:2048
	s_waitcnt vmcnt(9)
	ds_write_b128 v197, v[18:21] offset:35776
	s_waitcnt vmcnt(8)
	ds_write_b128 v198, v[44:47] offset:40896
	s_waitcnt vmcnt(7)
	ds_write_b128 v199, v[48:51] offset:46016
	s_waitcnt vmcnt(6)
	ds_write_b128 v200, v[52:55] offset:51136
	s_waitcnt vmcnt(5)
	ds_write_b128 v201, v[56:59] offset:56256
	v_mfma_f32_16x16x32_f16 v[14:17], v[172:175], v[156:159], v[14:17]
	v_mfma_f32_16x16x32_f16 v[2:5], v[160:163], v[60:63], v[2:5]
	v_mfma_f32_16x16x32_f16 v[6:9], v[164:167], v[60:63], v[6:9]
	v_mfma_f32_16x16x32_f16 v[10:13], v[184:187], v[60:63], v[10:13]
	v_mfma_f32_16x16x32_f16 v[14:17], v[168:171], v[60:63], v[14:17]
	v_mfma_f32_16x16x32_f16 v[2:5], v[176:179], v[152:155], v[2:5]
	v_mfma_f32_16x16x32_f16 v[6:9], v[180:183], v[152:155], v[6:9]
	v_mfma_f32_16x16x32_f16 v[10:13], v[188:191], v[152:155], v[10:13]
	v_mfma_f32_16x16x32_f16 v[14:17], v[192:195], v[152:155], v[14:17]
	ds_read_b128 v[60:63], v129 offset:35776
	ds_read_b128 v[152:155], v144 offset:1664
	ds_read_b128 v[208:211], v129 offset:42432
	ds_read_b128 v[212:215], v129 offset:49088
	ds_read_b128 v[216:219], v129 offset:55744
	ds_read_b128 v[156:159], v144 offset:1728
	ds_read_b128 v[160:163], v129 offset:35840
	ds_read_b128 v[164:167], v129 offset:42496
	ds_read_b128 v[168:171], v129 offset:49152
	ds_read_b128 v[172:175], v129 offset:55808
	s_waitcnt lgkmcnt(8)
	v_mfma_f32_16x16x32_f16 v[2:5], v[60:63], v[152:155], v[2:5]
	s_waitcnt lgkmcnt(7)
	v_mfma_f32_16x16x32_f16 v[6:9], v[208:211], v[152:155], v[6:9]
	s_waitcnt lgkmcnt(6)
	v_mfma_f32_16x16x32_f16 v[10:13], v[212:215], v[152:155], v[10:13]
	s_waitcnt lgkmcnt(5)
	v_mfma_f32_16x16x32_f16 v[14:17], v[216:219], v[152:155], v[14:17]
	s_waitcnt lgkmcnt(0)
	ds_read_b128 v[60:63], v129 offset:35904
	v_mfma_f32_16x16x32_f16 v[2:5], v[160:163], v[156:159], v[2:5]
	v_mfma_f32_16x16x32_f16 v[6:9], v[164:167], v[156:159], v[6:9]
	v_mfma_f32_16x16x32_f16 v[10:13], v[168:171], v[156:159], v[10:13]
	s_waitcnt lgkmcnt(1)
	v_mfma_f32_16x16x32_f16 v[14:17], v[172:175], v[156:159], v[14:17]
	ds_read_b128 v[152:155], v144 offset:1792
	ds_read_b128 v[208:211], v129 offset:42560
	ds_read_b128 v[212:215], v129 offset:49216
	ds_read_b128 v[216:219], v129 offset:55872
	ds_read_b128 v[156:159], v144 offset:1856
	ds_read_b128 v[160:163], v129 offset:35968
	ds_read_b128 v[164:167], v129 offset:42624
	ds_read_b128 v[168:171], v129 offset:49280
	ds_read_b128 v[172:175], v129 offset:55936
	s_waitcnt lgkmcnt(8)
	v_mfma_f32_16x16x32_f16 v[2:5], v[60:63], v[152:155], v[2:5]
	s_waitcnt lgkmcnt(7)
	v_mfma_f32_16x16x32_f16 v[6:9], v[208:211], v[152:155], v[6:9]
	s_waitcnt lgkmcnt(6)
	v_mfma_f32_16x16x32_f16 v[10:13], v[212:215], v[152:155], v[10:13]
	s_waitcnt lgkmcnt(5)
	v_mfma_f32_16x16x32_f16 v[14:17], v[216:219], v[152:155], v[14:17]
	s_waitcnt lgkmcnt(0)
	ds_read_b128 v[60:63], v129 offset:36032
	v_mfma_f32_16x16x32_f16 v[2:5], v[160:163], v[156:159], v[2:5]
	v_mfma_f32_16x16x32_f16 v[6:9], v[164:167], v[156:159], v[6:9]
	v_mfma_f32_16x16x32_f16 v[10:13], v[168:171], v[156:159], v[10:13]
	s_waitcnt lgkmcnt(1)
	v_mfma_f32_16x16x32_f16 v[14:17], v[172:175], v[156:159], v[14:17]
	ds_read_b128 v[152:155], v144 offset:1920
	ds_read_b128 v[156:159], v144 offset:1984
	ds_read_b128 v[160:163], v129 offset:36096
	s_waitcnt lgkmcnt(2)
	v_mfma_f32_16x16x32_f16 v[2:5], v[60:63], v[152:155], v[2:5]
	ds_read_b128 v[60:63], v129 offset:42688
	ds_read_b128 v[164:167], v129 offset:42752
	s_waitcnt lgkmcnt(1)
	v_mfma_f32_16x16x32_f16 v[6:9], v[60:63], v[152:155], v[6:9]
	ds_read_b128 v[60:63], v129 offset:49344
	ds_read_b128 v[168:171], v129 offset:49408
	s_waitcnt lgkmcnt(1)
	v_mfma_f32_16x16x32_f16 v[10:13], v[60:63], v[152:155], v[10:13]
	ds_read_b128 v[60:63], v129 offset:56000
	ds_read_b128 v[172:175], v129 offset:56064
	s_waitcnt lgkmcnt(0)
	v_mfma_f32_16x16x32_f16 v[14:17], v[60:63], v[152:155], v[14:17]
	v_mfma_f32_16x16x32_f16 v[2:5], v[160:163], v[156:159], v[2:5]
	s_waitcnt lgkmcnt(0)
	s_barrier
	s_waitcnt vmcnt(4)
	ds_write_b128 v123, v[24:27] offset:35776
	s_waitcnt vmcnt(3)
	ds_write_b128 v124, v[28:31] offset:40896
	s_waitcnt vmcnt(2)
	ds_write_b128 v125, v[32:35] offset:46016
	s_waitcnt vmcnt(1)
	ds_write_b128 v126, v[36:39] offset:51136
	s_waitcnt vmcnt(0)
	ds_write_b128 v127, v[40:43] offset:56256
	v_mfma_f32_16x16x32_f16 v[6:9], v[164:167], v[156:159], v[6:9]
	v_mfma_f32_16x16x32_f16 v[10:13], v[168:171], v[156:159], v[10:13]
	v_mfma_f32_16x16x32_f16 v[14:17], v[172:175], v[156:159], v[14:17]
	ds_read_b128 v[18:21], v196 offset:35776
	ds_read_b128 v[44:47], v144 offset:2080
	ds_read_b128 v[48:51], v144 offset:2144
	ds_read_b128 v[52:55], v196 offset:35840
	s_waitcnt lgkmcnt(2)
	v_mfma_f32_16x16x32_f16 v[2:5], v[18:21], v[44:47], v[2:5]
	ds_read_b128 v[18:21], v196 offset:42432
	ds_read_b128 v[56:59], v196 offset:42496
	s_waitcnt lgkmcnt(1)
	v_mfma_f32_16x16x32_f16 v[6:9], v[18:21], v[44:47], v[6:9]
	ds_read_b128 v[18:21], v196 offset:49088
	ds_read_b128 v[60:63], v196 offset:49152
	s_waitcnt lgkmcnt(1)
	v_mfma_f32_16x16x32_f16 v[10:13], v[18:21], v[44:47], v[10:13]
	ds_read_b128 v[18:21], v196 offset:55744
	ds_read_b128 v[152:155], v196 offset:55808
	s_waitcnt lgkmcnt(1)
	v_mfma_f32_16x16x32_f16 v[14:17], v[18:21], v[44:47], v[14:17]
	ds_read_b128 v[18:21], v196 offset:35904
	v_mfma_f32_16x16x32_f16 v[2:5], v[52:55], v[48:51], v[2:5]
	v_mfma_f32_16x16x32_f16 v[6:9], v[56:59], v[48:51], v[6:9]
	v_mfma_f32_16x16x32_f16 v[10:13], v[60:63], v[48:51], v[10:13]
	s_waitcnt lgkmcnt(1)
	v_mfma_f32_16x16x32_f16 v[14:17], v[152:155], v[48:51], v[14:17]
	ds_read_b128 v[44:47], v144 offset:2208
	ds_read_b128 v[48:51], v144 offset:2272
	ds_read_b128 v[52:55], v196 offset:35968
	s_waitcnt lgkmcnt(2)
	v_mfma_f32_16x16x32_f16 v[2:5], v[18:21], v[44:47], v[2:5]
	ds_read_b128 v[18:21], v196 offset:42560
	ds_read_b128 v[56:59], v196 offset:42624
	s_waitcnt lgkmcnt(1)
	v_mfma_f32_16x16x32_f16 v[6:9], v[18:21], v[44:47], v[6:9]
	ds_read_b128 v[18:21], v196 offset:49216
	ds_read_b128 v[60:63], v196 offset:49280
	s_waitcnt lgkmcnt(1)
	v_mfma_f32_16x16x32_f16 v[10:13], v[18:21], v[44:47], v[10:13]
	ds_read_b128 v[18:21], v196 offset:55872
	ds_read_b128 v[152:155], v196 offset:55936
	s_waitcnt lgkmcnt(1)
	v_mfma_f32_16x16x32_f16 v[14:17], v[18:21], v[44:47], v[14:17]
	ds_read_b128 v[18:21], v196 offset:36032
	v_mfma_f32_16x16x32_f16 v[2:5], v[52:55], v[48:51], v[2:5]
	v_mfma_f32_16x16x32_f16 v[6:9], v[56:59], v[48:51], v[6:9]
	v_mfma_f32_16x16x32_f16 v[10:13], v[60:63], v[48:51], v[10:13]
	s_waitcnt lgkmcnt(1)
	v_mfma_f32_16x16x32_f16 v[14:17], v[152:155], v[48:51], v[14:17]
	ds_read_b128 v[44:47], v144 offset:2336
	ds_read_b128 v[48:51], v144 offset:2400
	ds_read_b128 v[52:55], v196 offset:36096
	s_waitcnt lgkmcnt(2)
	v_mfma_f32_16x16x32_f16 v[2:5], v[18:21], v[44:47], v[2:5]
	ds_read_b128 v[18:21], v196 offset:42688
	ds_read_b128 v[56:59], v196 offset:42752
	s_waitcnt lgkmcnt(1)
	v_mfma_f32_16x16x32_f16 v[6:9], v[18:21], v[44:47], v[6:9]
	ds_read_b128 v[18:21], v196 offset:49344
	ds_read_b128 v[60:63], v196 offset:49408
	s_waitcnt lgkmcnt(1)
	v_mfma_f32_16x16x32_f16 v[10:13], v[18:21], v[44:47], v[10:13]
	ds_read_b128 v[18:21], v196 offset:56000
	ds_read_b128 v[152:155], v196 offset:56064
	s_waitcnt lgkmcnt(0)
	v_mfma_f32_16x16x32_f16 v[14:17], v[18:21], v[44:47], v[14:17]
	v_mfma_f32_16x16x32_f16 v[2:5], v[52:55], v[48:51], v[2:5]
	s_waitcnt lgkmcnt(0)
	s_barrier
	v_mfma_f32_16x16x32_f16 v[6:9], v[56:59], v[48:51], v[6:9]
	v_mfma_f32_16x16x32_f16 v[10:13], v[60:63], v[48:51], v[10:13]
	v_mfma_f32_16x16x32_f16 v[14:17], v[152:155], v[48:51], v[14:17]
	ds_read_b128 v[18:21], v129 offset:35776
	ds_read_b128 v[22:25], v144 offset:2496
	ds_read_b128 v[26:29], v144 offset:2560
	ds_read_b128 v[30:33], v129 offset:35840
	s_waitcnt lgkmcnt(2)
	v_mfma_f32_16x16x32_f16 v[2:5], v[18:21], v[22:25], v[2:5]
	ds_read_b128 v[18:21], v129 offset:42432
	ds_read_b128 v[34:37], v129 offset:42496
	s_waitcnt lgkmcnt(1)
	v_mfma_f32_16x16x32_f16 v[6:9], v[18:21], v[22:25], v[6:9]
	ds_read_b128 v[18:21], v129 offset:49088
	ds_read_b128 v[38:41], v129 offset:49152
	s_waitcnt lgkmcnt(1)
	v_mfma_f32_16x16x32_f16 v[10:13], v[18:21], v[22:25], v[10:13]
	ds_read_b128 v[18:21], v129 offset:55744
	ds_read_b128 v[42:45], v129 offset:55808
	s_waitcnt lgkmcnt(1)
	v_mfma_f32_16x16x32_f16 v[14:17], v[18:21], v[22:25], v[14:17]
	v_mfma_f32_16x16x32_f16 v[2:5], v[30:33], v[26:29], v[2:5]
	ds_read_b128 v[18:21], v144 offset:2624
	ds_read_b128 v[22:25], v144 offset:2688
	ds_read_b128 v[30:33], v129 offset:35904
	ds_read_b128 v[46:49], v129 offset:35968
	s_waitcnt lgkmcnt(1)
	v_mfma_f32_16x16x32_f16 v[2:5], v[30:33], v[18:21], v[2:5]
	v_mfma_f32_16x16x32_f16 v[6:9], v[34:37], v[26:29], v[6:9]
	ds_read_b128 v[34:37], v129 offset:42560
	ds_read_b128 v[50:53], v129 offset:42624
	ds_read_b128 v[54:57], v129 offset:49216
	ds_read_b128 v[58:61], v129 offset:49280
	v_mfma_f32_16x16x32_f16 v[10:13], v[38:41], v[26:29], v[10:13]
	ds_read_b128 v[38:41], v129 offset:55872
	ds_read_b128 v[62:65], v129 offset:55936
	ds_read_b128 v[152:155], v129 offset:36032
	ds_read_b128 v[30:33], v144 offset:2752
	ds_read_b128 v[156:159], v144 offset:2816
	ds_read_b128 v[160:163], v129 offset:36096
	s_waitcnt lgkmcnt(10)
	v_mfma_f32_16x16x32_f16 v[2:5], v[46:49], v[22:25], v[2:5]
	ds_read_b128 v[46:49], v129 offset:42688
	ds_read_b128 v[164:167], v129 offset:42752
	ds_read_b128 v[168:171], v129 offset:49344
	ds_read_b128 v[172:175], v129 offset:49408
	s_waitcnt lgkmcnt(6)
	v_mfma_f32_16x16x32_f16 v[2:5], v[152:155], v[30:33], v[2:5]
	ds_read_b128 v[152:155], v129 offset:56000
	ds_read_b128 v[176:179], v129 offset:56064
	ds_read_b128 v[180:183], v98 offset:63808
	ds_read_b128 v[184:187], v98 offset:64064
	s_waitcnt lgkmcnt(8)
	v_mfma_f32_16x16x32_f16 v[2:5], v[160:163], v[156:159], v[2:5]
	ds_read_b128 v[160:163], v98 offset:63872
	ds_read_b128 v[188:191], v98 offset:64128
	v_mfma_f32_16x16x32_f16 v[14:17], v[42:45], v[26:29], v[14:17]
	s_waitcnt lgkmcnt(2)
	s_nop 3
	v_pk_fma_f32 v[2:3], v[2:3], v[180:181], v[184:185]
	s_nop 0
	v_pk_mul_f32 v[26:27], v[2:3], s[28:29] op_sel_hi:[1,0]
	v_mfma_f32_16x16x32_f16 v[6:9], v[34:37], v[18:21], v[6:9]
	v_mul_f32_e64 v29, |v26|, -|v26|
	v_mul_f32_e32 v29, 0x3fb8aa3b, v29
	v_fma_f32 v28, |v26|, s74, 1.0
	v_exp_f32_e32 v34, v29
	v_fma_f32 v29, |v27|, s74, 1.0
	v_rcp_f32_e32 v28, v28
	v_rcp_f32_e32 v29, v29
	v_mfma_f32_16x16x32_f16 v[10:13], v[54:57], v[18:21], v[10:13]
	v_mul_f32_e64 v35, |v27|, -|v27|
	v_mul_f32_e32 v35, 0x3fb8aa3b, v35
	v_exp_f32_e32 v35, v35
	v_mfma_f32_16x16x32_f16 v[16:19], v[38:41], v[18:21], v[14:17]
	v_mul_f32_e64 v2, v2, 0.5
	v_mul_f32_e64 v3, v3, 0.5
	s_nop 0
	v_mov_b64_e32 v[14:15], s[34:35]
	v_pk_fma_f32 v[20:21], v[28:29], s[40:41], v[14:15] op_sel_hi:[1,0,0]
	v_mfma_f32_16x16x32_f16 v[10:13], v[58:61], v[22:25], v[10:13]
	v_fma_f32 v20, v28, v20, s42
	v_fma_f32 v21, v29, v21, s42
	v_pk_fma_f32 v[20:21], v[28:29], v[20:21], s[44:45] op_sel_hi:[1,1,0]
	v_mfma_f32_16x16x32_f16 v[6:9], v[50:53], v[22:25], v[6:9]
	v_fma_f32 v20, v28, v20, s46
	v_fma_f32 v21, v29, v21, s46
	v_pk_mul_f32 v[20:21], v[20:21], v[28:29] neg_lo:[0,1] neg_hi:[0,1]
	v_mfma_f32_16x16x32_f16 v[16:19], v[62:65], v[22:25], v[16:19]
	v_fma_f32 v20, v20, v34, 1.0
	v_fma_f32 v21, v21, v35, 1.0
	v_bfi_b32 v21, s71, v21, v27
	v_bfi_b32 v20, s71, v20, v26
	v_pk_fma_f32 v[26:27], v[4:5], v[182:183], v[186:187]
	v_pk_add_f32 v[20:21], v[20:21], 1.0 op_sel_hi:[1,0]
	v_pk_mul_f32 v[28:29], v[26:27], s[28:29] op_sel_hi:[1,0]
	v_pk_mul_f32 v[24:25], v[2:3], v[20:21]
	v_mfma_f32_16x16x32_f16 v[2:5], v[168:171], v[30:33], v[10:13]
	v_mul_f32_e64 v26, v26, 0.5
	v_mul_f32_e64 v27, v27, 0.5
	s_nop 0
	v_fma_f32 v10, |v28|, s74, 1.0
	v_fma_f32 v11, |v29|, s74, 1.0
	v_rcp_f32_e32 v34, v10
	v_rcp_f32_e32 v35, v11
	v_mul_f32_e64 v10, |v28|, -|v28|
	v_mul_f32_e32 v10, 0x3fb8aa3b, v10
	v_mfma_f32_16x16x32_f16 v[6:9], v[46:49], v[30:33], v[6:9]
	v_mfma_f32_16x16x32_f16 v[16:19], v[152:155], v[30:33], v[16:19]
	v_exp_f32_e32 v30, v10
	v_mfma_f32_16x16x32_f16 v[10:13], v[172:175], v[156:159], v[2:5]
	s_nop 2
	v_mul_f32_e64 v4, |v29|, -|v29|
	v_pk_fma_f32 v[2:3], v[34:35], s[40:41], v[14:15] op_sel_hi:[1,0,0]
	v_mul_f32_e32 v4, 0x3fb8aa3b, v4
	v_pk_fma_f32 v[2:3], v[34:35], v[2:3], s[42:43] op_sel_hi:[1,1,0]
	v_exp_f32_e32 v31, v4
	v_pk_fma_f32 v[2:3], v[34:35], v[2:3], s[44:45] op_sel_hi:[1,1,0]
	v_mfma_f32_16x16x32_f16 v[20:23], v[164:167], v[156:159], v[6:9]
	v_fma_f32 v2, v34, v2, s46
	v_fma_f32 v3, v35, v3, s46
	v_pk_mul_f32 v[2:3], v[2:3], v[34:35] neg_lo:[0,1] neg_hi:[0,1]
	v_mfma_f32_16x16x32_f16 v[6:9], v[176:179], v[156:159], v[16:19]
	v_fma_f32 v2, v2, v30, 1.0
	v_fma_f32 v3, v3, v31, 1.0
	v_bfi_b32 v3, s71, v3, v29
	v_bfi_b32 v2, s71, v2, v28
	v_pk_add_f32 v[2:3], v[2:3], 1.0 op_sel_hi:[1,0]
	s_nop 0
	v_pk_mul_f32 v[4:5], v[26:27], v[2:3]
	v_cvt_pk_f16_f32 v2, v24, v25
	v_cvt_pk_f16_f32 v3, v4, v5
	s_waitcnt lgkmcnt(0)
	v_pk_fma_f32 v[4:5], v[20:21], v[160:161], v[188:189]
	s_nop 0
	v_pk_mul_f32 v[16:17], v[4:5], s[28:29] op_sel_hi:[1,0]
	v_pk_mul_f32 v[4:5], v[4:5], 0.5 op_sel_hi:[1,0]
	v_fma_f32 v18, |v16|, s74, 1.0
	v_fma_f32 v19, |v17|, s74, 1.0
	v_rcp_f32_e32 v18, v18
	v_rcp_f32_e32 v19, v19
	v_mul_f32_e64 v20, |v16|, -|v16|
	v_mul_f32_e64 v21, |v17|, -|v17|
	v_mul_f32_e32 v20, 0x3fb8aa3b, v20
	v_pk_fma_f32 v[24:25], v[18:19], s[40:41], v[14:15] op_sel_hi:[1,0,0]
	v_mul_f32_e32 v21, 0x3fb8aa3b, v21
	v_exp_f32_e32 v20, v20
	v_pk_fma_f32 v[24:25], v[18:19], v[24:25], s[42:43] op_sel_hi:[1,1,0]
	v_exp_f32_e32 v21, v21
	v_pk_fma_f32 v[24:25], v[18:19], v[24:25], s[44:45] op_sel_hi:[1,1,0]
	s_nop 0
	v_pk_fma_f32 v[24:25], v[18:19], v[24:25], s[46:47] op_sel_hi:[1,1,0]
	s_nop 0
	v_pk_mul_f32 v[18:19], v[24:25], v[18:19] neg_lo:[0,1] neg_hi:[0,1]
	s_nop 0
	v_pk_fma_f32 v[18:19], v[18:19], v[20:21], 1.0 op_sel_hi:[1,1,0]
	s_nop 0
	v_bfi_b32 v17, s71, v19, v17
	v_bfi_b32 v16, s71, v18, v16
	v_pk_add_f32 v[16:17], v[16:17], 1.0 op_sel_hi:[1,0]
	s_nop 0
	v_pk_mul_f32 v[4:5], v[4:5], v[16:17]
	v_pk_fma_f32 v[16:17], v[22:23], v[162:163], v[190:191]
	v_cvt_pk_f16_f32 v4, v4, v5
	v_pk_mul_f32 v[18:19], v[16:17], s[28:29] op_sel_hi:[1,0]
	v_pk_mul_f32 v[16:17], v[16:17], 0.5 op_sel_hi:[1,0]
	v_fma_f32 v20, |v18|, s74, 1.0
	v_fma_f32 v21, |v19|, s74, 1.0
	v_rcp_f32_e32 v20, v20
	v_rcp_f32_e32 v21, v21
	v_mul_f32_e64 v22, |v18|, -|v18|
	v_mul_f32_e64 v23, |v19|, -|v19|
	v_mul_f32_e32 v22, 0x3fb8aa3b, v22
	v_pk_fma_f32 v[24:25], v[20:21], s[40:41], v[14:15] op_sel_hi:[1,0,0]
	v_mul_f32_e32 v23, 0x3fb8aa3b, v23
	v_exp_f32_e32 v22, v22
	v_pk_fma_f32 v[24:25], v[20:21], v[24:25], s[42:43] op_sel_hi:[1,1,0]
	v_exp_f32_e32 v23, v23
	v_pk_fma_f32 v[24:25], v[20:21], v[24:25], s[44:45] op_sel_hi:[1,1,0]
	s_nop 0
	v_pk_fma_f32 v[24:25], v[20:21], v[24:25], s[46:47] op_sel_hi:[1,1,0]
	s_nop 0
	v_pk_mul_f32 v[20:21], v[24:25], v[20:21] neg_lo:[0,1] neg_hi:[0,1]
	s_nop 0
	v_pk_fma_f32 v[20:21], v[20:21], v[22:23], 1.0 op_sel_hi:[1,1,0]
	s_nop 0
	v_bfi_b32 v19, s71, v21, v19
	v_bfi_b32 v18, s71, v20, v18
	v_pk_add_f32 v[18:19], v[18:19], 1.0 op_sel_hi:[1,0]
	s_nop 0
	v_pk_mul_f32 v[16:17], v[16:17], v[18:19]
	ds_read_b128 v[18:21], v98 offset:63936
	ds_read_b128 v[22:25], v98 offset:64192
	v_cvt_pk_f16_f32 v5, v16, v17
	ds_read_b128 v[26:29], v98 offset:64000
	ds_read_b128 v[30:33], v98 offset:64256
	s_waitcnt lgkmcnt(2)
	v_pk_fma_f32 v[10:11], v[10:11], v[18:19], v[22:23]
	s_nop 0
	v_pk_mul_f32 v[22:23], v[10:11], s[28:29] op_sel_hi:[1,0]
	v_pk_fma_f32 v[12:13], v[12:13], v[20:21], v[24:25]
	v_fma_f32 v16, |v22|, s74, 1.0
	v_fma_f32 v17, |v23|, s74, 1.0
	v_rcp_f32_e32 v16, v16
	v_rcp_f32_e32 v17, v17
	v_mul_f32_e64 v18, |v22|, -|v22|
	v_mul_f32_e64 v19, |v23|, -|v23|
	v_mul_f32_e32 v18, 0x3fb8aa3b, v18
	v_pk_fma_f32 v[34:35], v[16:17], s[40:41], v[14:15] op_sel_hi:[1,0,0]
	v_mul_f32_e32 v19, 0x3fb8aa3b, v19
	v_exp_f32_e32 v18, v18
	v_pk_fma_f32 v[34:35], v[16:17], v[34:35], s[42:43] op_sel_hi:[1,1,0]
	v_exp_f32_e32 v19, v19
	v_pk_fma_f32 v[34:35], v[16:17], v[34:35], s[44:45] op_sel_hi:[1,1,0]
	v_pk_mul_f32 v[10:11], v[10:11], 0.5 op_sel_hi:[1,0]
	v_pk_fma_f32 v[34:35], v[16:17], v[34:35], s[46:47] op_sel_hi:[1,1,0]
	v_pk_mul_f32 v[20:21], v[12:13], s[28:29] op_sel_hi:[1,0]
	v_pk_mul_f32 v[16:17], v[34:35], v[16:17] neg_lo:[0,1] neg_hi:[0,1]
	v_mul_f32_e64 v24, |v20|, -|v20|
	v_pk_fma_f32 v[46:47], v[16:17], v[18:19], 1.0 op_sel_hi:[1,1,0]
	v_lshl_add_u64 v[18:19], s[50:51], 1, v[100:101]
	global_load_dwordx4 v[34:37], v[18:19], off
	global_load_dwordx4 v[42:45], v[18:19], off offset:1024
	v_lshl_add_u64 v[16:17], s[50:51], 2, v[102:103]
	global_load_dwordx4 v[38:41], v[16:17], off
	v_mov_b32_e32 v190, 0x1000
	v_mov_b32_e32 v191, 0
	global_load_dwordx4 v[152:155], v[18:19], off offset:2048
	global_load_dwordx4 v[156:159], v[18:19], off offset:3072
	global_load_dwordx4 v[160:163], v[16:17], off offset:64
	v_lshl_add_u64 v[188:189], v[18:19], 0, v[190:191]
	global_load_dwordx4 v[164:167], v[188:189], off
	global_load_dwordx4 v[168:171], v[188:189], off offset:1024
	global_load_dwordx4 v[172:175], v[16:17], off offset:128
	global_load_dwordx4 v[176:179], v[188:189], off offset:2048
	global_load_dwordx4 v[180:183], v[188:189], off offset:3072
	global_load_dwordx4 v[184:187], v[16:17], off offset:192
	v_bfi_b32 v23, s71, v47, v23
	v_bfi_b32 v22, s71, v46, v22
	v_pk_add_f32 v[22:23], v[22:23], 1.0 op_sel_hi:[1,0]
	v_mul_f32_e64 v25, |v21|, -|v21|
	v_pk_mul_f32 v[10:11], v[10:11], v[22:23]
	v_fma_f32 v22, |v20|, s74, 1.0
	v_fma_f32 v23, |v21|, s74, 1.0
	v_rcp_f32_e32 v22, v22
	v_rcp_f32_e32 v23, v23
	v_mul_f32_e32 v24, 0x3fb8aa3b, v24
	v_mul_f32_e32 v25, 0x3fb8aa3b, v25
	v_exp_f32_e32 v24, v24
	v_pk_fma_f32 v[46:47], v[22:23], s[40:41], v[14:15] op_sel_hi:[1,0,0]
	v_exp_f32_e32 v25, v25
	v_pk_fma_f32 v[46:47], v[22:23], v[46:47], s[42:43] op_sel_hi:[1,1,0]
	v_pk_mul_f32 v[12:13], v[12:13], 0.5 op_sel_hi:[1,0]
	v_pk_fma_f32 v[46:47], v[22:23], v[46:47], s[44:45] op_sel_hi:[1,1,0]
	s_waitcnt lgkmcnt(0)
	v_pk_fma_f32 v[6:7], v[6:7], v[26:27], v[30:31]
	v_pk_fma_f32 v[46:47], v[22:23], v[46:47], s[46:47] op_sel_hi:[1,1,0]
	v_cvt_pk_f16_f32 v10, v10, v11
	v_pk_mul_f32 v[22:23], v[46:47], v[22:23] neg_lo:[0,1] neg_hi:[0,1]
	v_pk_fma_f32 v[8:9], v[8:9], v[28:29], v[32:33]
	v_pk_fma_f32 v[22:23], v[22:23], v[24:25], 1.0 op_sel_hi:[1,1,0]
	s_mul_i32 s50, s94, 0xfef85000
	v_bfi_b32 v21, s71, v23, v21
	v_bfi_b32 v20, s71, v22, v20
	v_pk_add_f32 v[20:21], v[20:21], 1.0 op_sel_hi:[1,0]
	s_nop 0
	v_pk_mul_f32 v[12:13], v[12:13], v[20:21]
	s_nop 0
	v_cvt_pk_f16_f32 v11, v12, v13
	v_pk_mul_f32 v[12:13], v[6:7], s[28:29] op_sel_hi:[1,0]
	v_pk_mul_f32 v[6:7], v[6:7], 0.5 op_sel_hi:[1,0]
	v_fma_f32 v20, |v12|, s74, 1.0
	v_fma_f32 v21, |v13|, s74, 1.0
	v_rcp_f32_e32 v20, v20
	v_rcp_f32_e32 v21, v21
	v_mul_f32_e64 v22, |v12|, -|v12|
	v_mul_f32_e64 v23, |v13|, -|v13|
	v_mul_f32_e32 v22, 0x3fb8aa3b, v22
	v_pk_fma_f32 v[24:25], v[20:21], s[40:41], v[14:15] op_sel_hi:[1,0,0]
	v_mul_f32_e32 v23, 0x3fb8aa3b, v23
	v_exp_f32_e32 v22, v22
	v_pk_fma_f32 v[24:25], v[20:21], v[24:25], s[42:43] op_sel_hi:[1,1,0]
	v_exp_f32_e32 v23, v23
	v_pk_fma_f32 v[24:25], v[20:21], v[24:25], s[44:45] op_sel_hi:[1,1,0]
	s_nop 0
	v_pk_fma_f32 v[24:25], v[20:21], v[24:25], s[46:47] op_sel_hi:[1,1,0]
	s_nop 0
	v_pk_mul_f32 v[20:21], v[24:25], v[20:21] neg_lo:[0,1] neg_hi:[0,1]
	s_nop 0
	v_pk_fma_f32 v[20:21], v[20:21], v[22:23], 1.0 op_sel_hi:[1,1,0]
	s_nop 0
	v_bfi_b32 v13, s71, v21, v13
	v_bfi_b32 v12, s71, v20, v12
	v_pk_add_f32 v[12:13], v[12:13], 1.0 op_sel_hi:[1,0]
	s_nop 0
	v_pk_mul_f32 v[6:7], v[6:7], v[12:13]
	v_pk_mul_f32 v[12:13], v[8:9], s[28:29] op_sel_hi:[1,0]
	v_pk_mul_f32 v[8:9], v[8:9], 0.5 op_sel_hi:[1,0]
	v_fma_f32 v20, |v12|, s74, 1.0
	v_fma_f32 v21, |v13|, s74, 1.0
	v_rcp_f32_e32 v20, v20
	v_rcp_f32_e32 v21, v21
	v_mul_f32_e64 v22, |v12|, -|v12|
	v_mul_f32_e64 v23, |v13|, -|v13|
	v_mul_f32_e32 v22, 0x3fb8aa3b, v22
	v_pk_fma_f32 v[14:15], v[20:21], s[40:41], v[14:15] op_sel_hi:[1,0,0]
	v_mul_f32_e32 v23, 0x3fb8aa3b, v23
	v_exp_f32_e32 v22, v22
	v_pk_fma_f32 v[14:15], v[20:21], v[14:15], s[42:43] op_sel_hi:[1,1,0]
	v_exp_f32_e32 v23, v23
	v_pk_fma_f32 v[14:15], v[20:21], v[14:15], s[44:45] op_sel_hi:[1,1,0]
	s_nop 0
	v_pk_fma_f32 v[14:15], v[20:21], v[14:15], s[46:47] op_sel_hi:[1,1,0]
	s_nop 0
	v_pk_mul_f32 v[14:15], v[14:15], v[20:21] neg_lo:[0,1] neg_hi:[0,1]
	s_nop 0
	v_pk_fma_f32 v[14:15], v[14:15], v[22:23], 1.0 op_sel_hi:[1,1,0]
	s_nop 0
	v_bfi_b32 v13, s71, v15, v13
	v_bfi_b32 v12, s71, v14, v12
	v_pk_add_f32 v[12:13], v[12:13], 1.0 op_sel_hi:[1,0]
	v_add_u32_e32 v14, s95, v128
	v_pk_mul_f32 v[8:9], v[8:9], v[12:13]
	v_cvt_pk_f16_f32 v12, v6, v7
	v_cvt_pk_f16_f32 v13, v8, v9
	s_waitcnt vmcnt(0)
	v_pk_mul_f32 v[8:9], v[40:41], s[48:49] op_sel_hi:[1,0]
	v_pk_mul_f32 v[6:7], v[38:39], s[48:49] op_sel_hi:[1,0]
	v_cmp_gt_i32_e64 s[20:21], s73, v14
	v_add_u32_e32 v14, s50, v134
	v_mfma_f32_16x16x32_f16 v[6:9], v[34:37], v[2:5], v[6:9]
	v_mfma_f32_16x16x32_f16 v[6:9], v[42:45], v[10:13], v[6:9]
	v_pk_mul_f32 v[160:161], v[160:161], s[48:49] op_sel_hi:[1,0]
	v_pk_mul_f32 v[162:163], v[162:163], s[48:49] op_sel_hi:[1,0]
	v_pk_mul_f32 v[172:173], v[172:173], s[48:49] op_sel_hi:[1,0]
	v_pk_mul_f32 v[174:175], v[174:175], s[48:49] op_sel_hi:[1,0]
	v_pk_mul_f32 v[184:185], v[184:185], s[48:49] op_sel_hi:[1,0]
	v_pk_mul_f32 v[186:187], v[186:187], s[48:49] op_sel_hi:[1,0]
	s_nop 1
	v_mfma_f32_16x16x32_f16 v[20:23], v[152:155], v[2:5], v[160:163]
	v_mfma_f32_16x16x32_f16 v[24:27], v[164:167], v[2:5], v[172:175]
	v_mfma_f32_16x16x32_f16 v[28:31], v[176:179], v[2:5], v[184:187]
	v_mfma_f32_16x16x32_f16 v[20:23], v[156:159], v[10:13], v[20:23]
	v_mfma_f32_16x16x32_f16 v[24:27], v[168:171], v[10:13], v[24:27]
	v_mfma_f32_16x16x32_f16 v[28:31], v[180:183], v[10:13], v[28:31]
	s_and_saveexec_b64 s[50:51], s[20:21]
	s_cbranch_execz .Lmy_k2_nostore
	s_nop 7
	buffer_store_dwordx4 v[6:9], v14, s[24:27], 0 offen sc1
	buffer_store_dwordx4 v[20:23], v14, s[24:27], 0 offen offset:64 sc1
	buffer_store_dwordx4 v[24:27], v14, s[24:27], 0 offen offset:128 sc1
	buffer_store_dwordx4 v[28:31], v14, s[24:27], 0 offen offset:192 sc1

	.amdhsa_kernel _Z10k_enc_scanPKDF16_PKfS2_S2_S2_S2_S2_S2_S2_S2_S2_S0_S2_S2_S2_S2_S2_S0_S2_PfPjS2_S2_S2_S2_S2_S2_S2_S2_S2_S2_S2_S2_PDF16_S5_S3_
		.amdhsa_group_segment_fixed_size 91136
		.amdhsa_private_segment_fixed_size 0
		.amdhsa_kernarg_size 288
		.amdhsa_user_sgpr_count 2
		.amdhsa_user_sgpr_dispatch_ptr 0
		.amdhsa_user_sgpr_queue_ptr 0
		.amdhsa_user_sgpr_kernarg_segment_ptr 1
		.amdhsa_user_sgpr_dispatch_id 0
		.amdhsa_user_sgpr_kernarg_preload_length 0
		.amdhsa_user_sgpr_kernarg_preload_offset 0
		.amdhsa_user_sgpr_private_segment_size 0
		.amdhsa_uses_dynamic_stack 0
		.amdhsa_enable_private_segment 0
		.amdhsa_system_sgpr_workgroup_id_x 1
		.amdhsa_system_sgpr_workgroup_id_y 0
		.amdhsa_system_sgpr_workgroup_id_z 0
		.amdhsa_system_sgpr_workgroup_info 0
		.amdhsa_system_vgpr_workitem_id 0
		.amdhsa_next_free_vgpr 220
		.amdhsa_next_free_sgpr 98
		.amdhsa_accum_offset 220
		.amdhsa_reserve_vcc 1
		.amdhsa_float_round_mode_32 0
		.amdhsa_float_round_mode_16_64 0
		.amdhsa_float_denorm_mode_32 3
		.amdhsa_float_denorm_mode_16_64 3
		.amdhsa_dx10_clamp 1
		.amdhsa_ieee_mode 1
		.amdhsa_fp16_overflow 0
		.amdhsa_tg_split 0
		.amdhsa_exception_fp_ieee_invalid_op 0
		.amdhsa_exception_fp_denorm_src 0
		.amdhsa_exception_fp_ieee_div_zero 0
		.amdhsa_exception_fp_ieee_overflow 0
		.amdhsa_exception_fp_ieee_underflow 0
		.amdhsa_exception_fp_ieee_inexact 0
		.amdhsa_exception_int_div_zero 0
	.end_amdhsa_kernel

amdhsa.kernels:
  - .agpr_count:     8
    .args:
      - .actual_access:  read_only
        .address_space:  global
        .offset:         0
        .size:           8
        .value_kind:     global_buffer
      - .actual_access:  read_only
        .address_space:  global
        .offset:         8
        .size:           8
        .value_kind:     global_buffer
      - .actual_access:  write_only
        .address_space:  global
        .offset:         16
        .size:           8
        .value_kind:     global_buffer
      - .actual_access:  write_only
        .address_space:  global
        .offset:         24
        .size:           8
        .value_kind:     global_buffer
      - .actual_access:  read_only
        .address_space:  global
        .offset:         32
        .size:           8
        .value_kind:     global_buffer
      - .actual_access:  read_only
        .address_space:  global
        .offset:         40
        .size:           8
        .value_kind:     global_buffer
      - .actual_access:  write_only
        .address_space:  global
        .offset:         48
        .size:           8
        .value_kind:     global_buffer
      - .actual_access:  write_only
        .address_space:  global
        .offset:         56
        .size:           8
        .value_kind:     global_buffer
      - .actual_access:  write_only
        .address_space:  global
        .offset:         64
        .size:           8
        .value_kind:     global_buffer
    .group_segment_fixed_size: 24976
    .kernarg_segment_align: 8
    .kernarg_segment_size: 72
    .language:       OpenCL C
    .language_version:
      - 2
      - 0
    .max_flat_workgroup_size: 256
    .name:           _Z9k_fb_mfmaPKfS0_PDF16_PfS0_S0_S1_S1_Pj
    .private_segment_fixed_size: 0
    .sgpr_count:     24
    .sgpr_spill_count: 0
    .symbol:         _Z9k_fb_mfmaPKfS0_PDF16_PfS0_S0_S1_S1_Pj.kd
    .uniform_work_group_size: 1
    .uses_dynamic_stack: false
    .vgpr_count:     92
    .vgpr_spill_count: 0
    .wavefront_size: 64
  - .agpr_count:     0
    .args:
      - .actual_access:  read_only
        .address_space:  global
        .offset:         0
        .size:           8
        .value_kind:     global_buffer
      - .actual_access:  read_only
        .address_space:  global
        .offset:         8
        .size:           8
        .value_kind:     global_buffer
      - .actual_access:  write_only
        .address_space:  global
        .offset:         16
        .size:           8
        .value_kind:     global_buffer
      - .actual_access:  write_only
        .address_space:  global
        .offset:         24
        .size:           8
        .value_kind:     global_buffer
    .group_segment_fixed_size: 0
    .kernarg_segment_align: 8
    .kernarg_segment_size: 32
    .language:       OpenCL C
    .language_version:
      - 2
      - 0
    .max_flat_workgroup_size: 1024
    .name:           _Z6k_prepPKfS0_PDF16_S1_
    .private_segment_fixed_size: 0
    .sgpr_count:     19
    .sgpr_spill_count: 0
    .symbol:         _Z6k_prepPKfS0_PDF16_S1_.kd
    .uniform_work_group_size: 1
    .uses_dynamic_stack: false
    .vgpr_count:     8
    .vgpr_spill_count: 0
    .wavefront_size: 64
  - .agpr_count:     0
    .args:
      - .actual_access:  read_only
        .address_space:  global
        .offset:         0
        .size:           8
        .value_kind:     global_buffer
      - .actual_access:  read_only
        .address_space:  global
        .offset:         8
        .size:           8
        .value_kind:     global_buffer
      - .actual_access:  read_only
        .address_space:  global
        .offset:         16
        .size:           8
        .value_kind:     global_buffer
      - .actual_access:  read_only
        .address_space:  global
        .offset:         24
        .size:           8
        .value_kind:     global_buffer
      - .actual_access:  read_only
        .address_space:  global
        .offset:         32
        .size:           8
        .value_kind:     global_buffer
      - .actual_access:  read_only
        .address_space:  global
        .offset:         40
        .size:           8
        .value_kind:     global_buffer
      - .actual_access:  read_only
        .address_space:  global
        .offset:         48
        .size:           8
        .value_kind:     global_buffer
      - .actual_access:  read_only
        .address_space:  global
        .offset:         56
        .size:           8
        .value_kind:     global_buffer
      - .actual_access:  read_only
        .address_space:  global
        .offset:         64
        .size:           8
        .value_kind:     global_buffer
      - .actual_access:  read_only
        .address_space:  global
        .offset:         72
        .size:           8
        .value_kind:     global_buffer
      - .actual_access:  write_only
        .address_space:  global
        .offset:         80
        .size:           8
        .value_kind:     global_buffer
      - .actual_access:  write_only
        .address_space:  global
        .offset:         88
        .size:           8
        .value_kind:     global_buffer
    .group_segment_fixed_size: 236
    .kernarg_segment_align: 8
    .kernarg_segment_size: 96
    .language:       OpenCL C
    .language_version:
      - 2
      - 0
    .max_flat_workgroup_size: 192
    .name:           _Z6k_gatePKfS0_S0_S0_S0_S0_S0_S0_S0_S0_PfPj
    .private_segment_fixed_size: 0
    .sgpr_count:     32
    .sgpr_spill_count: 0
    .symbol:         _Z6k_gatePKfS0_S0_S0_S0_S0_S0_S0_S0_S0_PfPj.kd
    .uniform_work_group_size: 1
    .uses_dynamic_stack: false
    .vgpr_count:     47
    .vgpr_spill_count: 0
    .wavefront_size: 64
  - .agpr_count:     0
    .args:
      - .actual_access:  read_only
        .address_space:  global
        .offset:         0
        .size:           8
        .value_kind:     global_buffer
      - .actual_access:  read_only
        .address_space:  global
        .offset:         8
        .size:           8
        .value_kind:     global_buffer
      - .actual_access:  read_only
        .address_space:  global
        .offset:         16
        .size:           8
        .value_kind:     global_buffer
      - .actual_access:  read_only
        .address_space:  global
        .offset:         24
        .size:           8
        .value_kind:     global_buffer
      - .actual_access:  read_only
        .address_space:  global
        .offset:         32
        .size:           8
        .value_kind:     global_buffer
      - .actual_access:  read_only
        .address_space:  global
        .offset:         40
        .size:           8
        .value_kind:     global_buffer
      - .actual_access:  read_only
        .address_space:  global
        .offset:         48
        .size:           8
        .value_kind:     global_buffer
      - .actual_access:  read_only
        .address_space:  global
        .offset:         56
        .size:           8
        .value_kind:     global_buffer
      - .actual_access:  read_only
        .address_space:  global
        .offset:         64
        .size:           8
        .value_kind:     global_buffer
      - .actual_access:  read_only
        .address_space:  global
        .offset:         72
        .size:           8
        .value_kind:     global_buffer
      - .actual_access:  read_only
        .address_space:  global
        .offset:         80
        .size:           8
        .value_kind:     global_buffer
      - .actual_access:  read_only
        .address_space:  global
        .offset:         88
        .size:           8
        .value_kind:     global_buffer
      - .actual_access:  read_only
        .address_space:  global
        .offset:         96
        .size:           8
        .value_kind:     global_buffer
      - .actual_access:  read_only
        .address_space:  global
        .offset:         104
        .size:           8
        .value_kind:     global_buffer
      - .actual_access:  read_only
        .address_space:  global
        .offset:         112
        .size:           8
        .value_kind:     global_buffer
      - .actual_access:  read_only
        .address_space:  global
        .offset:         120
        .size:           8
        .value_kind:     global_buffer
      - .actual_access:  read_only
        .address_space:  global
        .offset:         128
        .size:           8
        .value_kind:     global_buffer
      - .actual_access:  read_only
        .address_space:  global
        .offset:         136
        .size:           8
        .value_kind:     global_buffer
      - .actual_access:  read_only
        .address_space:  global
        .offset:         144
        .size:           8
        .value_kind:     global_buffer
      - .address_space:  global
        .offset:         152
        .size:           8
        .value_kind:     global_buffer
      - .address_space:  global
        .offset:         160
        .size:           8
        .value_kind:     global_buffer
      - .actual_access:  read_only
        .address_space:  global
        .offset:         168
        .size:           8
        .value_kind:     global_buffer
      - .actual_access:  read_only
        .address_space:  global
        .offset:         176
        .size:           8
        .value_kind:     global_buffer
      - .actual_access:  read_only
        .address_space:  global
        .offset:         184
        .size:           8
        .value_kind:     global_buffer
      - .actual_access:  read_only
        .address_space:  global
        .offset:         192
        .size:           8
        .value_kind:     global_buffer
      - .actual_access:  read_only
        .address_space:  global
        .offset:         200
        .size:           8
        .value_kind:     global_buffer
      - .actual_access:  read_only
        .address_space:  global
        .offset:         208
        .size:           8
        .value_kind:     global_buffer
      - .actual_access:  read_only
        .address_space:  global
        .offset:         216
        .size:           8
        .value_kind:     global_buffer
      - .actual_access:  read_only
        .address_space:  global
        .offset:         224
        .size:           8
        .value_kind:     global_buffer
      - .actual_access:  read_only
        .address_space:  global
        .offset:         232
        .size:           8
        .value_kind:     global_buffer
      - .actual_access:  read_only
        .address_space:  global
        .offset:         240
        .size:           8
        .value_kind:     global_buffer
      - .actual_access:  read_only
        .address_space:  global
        .offset:         248
        .size:           8
        .value_kind:     global_buffer
      - .actual_access:  read_only
        .address_space:  global
        .offset:         256
        .size:           8
        .value_kind:     global_buffer
      - .actual_access:  write_only
        .address_space:  global
        .offset:         264
        .size:           8
        .value_kind:     global_buffer
      - .actual_access:  write_only
        .address_space:  global
        .offset:         272
        .size:           8
        .value_kind:     global_buffer
      - .actual_access:  write_only
        .address_space:  global
        .offset:         280
        .size:           8
        .value_kind:     global_buffer
    .group_segment_fixed_size: 91136
    .kernarg_segment_align: 8
    .kernarg_segment_size: 288
    .language:       OpenCL C
    .language_version:
      - 2
      - 0
    .max_flat_workgroup_size: 320
    .name:           _Z10k_enc_scanPKDF16_PKfS2_S2_S2_S2_S2_S2_S2_S2_S2_S0_S2_S2_S2_S2_S2_S0_S2_PfPjS2_S2_S2_S2_S2_S2_S2_S2_S2_S2_S2_S2_PDF16_S5_S3_
    .private_segment_fixed_size: 0
    .sgpr_count:     104
    .sgpr_spill_count: 0
    .symbol:         _Z10k_enc_scanPKDF16_PKfS2_S2_S2_S2_S2_S2_S2_S2_S2_S0_S2_S2_S2_S2_S2_S0_S2_PfPjS2_S2_S2_S2_S2_S2_S2_S2_S2_S2_S2_S2_PDF16_S5_S3_.kd
    .uniform_work_group_size: 1
    .uses_dynamic_stack: false
    .vgpr_count:     220
    .vgpr_spill_count: 0
    .wavefront_size: 64
  - .agpr_count:     0
    .args:
      - .actual_access:  read_only
        .address_space:  global
        .offset:         0
        .size:           8
        .value_kind:     global_buffer
      - .actual_access:  read_only
        .address_space:  global
        .offset:         8
        .size:           8
        .value_kind:     global_buffer
      - .actual_access:  write_only
        .address_space:  global
        .offset:         16
        .size:           8
        .value_kind:     global_buffer
    .group_segment_fixed_size: 66580
    .kernarg_segment_align: 8
    .kernarg_segment_size: 24
    .language:       OpenCL C
    .language_version:
      - 2
      - 0
    .max_flat_workgroup_size: 320
    .name:           _Z7k_att1nPKDF16_S0_Pf
    .private_segment_fixed_size: 0
    .sgpr_count:     29
    .sgpr_spill_count: 0
    .symbol:         _Z7k_att1nPKDF16_S0_Pf.kd
    .uniform_work_group_size: 1
    .uses_dynamic_stack: false
    .vgpr_count:     126
    .vgpr_spill_count: 0
    .wavefront_size: 64
  - .agpr_count:     0
    .args:
      - .actual_access:  read_only
        .address_space:  global
        .offset:         0
        .size:           8
        .value_kind:     global_buffer
      - .actual_access:  read_only
        .address_space:  global
        .offset:         8
        .size:           8
        .value_kind:     global_buffer
      - .actual_access:  read_only
        .address_space:  global
        .offset:         16
        .size:           8
        .value_kind:     global_buffer
      - .actual_access:  write_only
        .address_space:  global
        .offset:         24
        .size:           8
        .value_kind:     global_buffer
      - .actual_access:  read_only
        .address_space:  global
        .offset:         32
        .size:           8
        .value_kind:     global_buffer
      - .actual_access:  read_only
        .address_space:  global
        .offset:         40
        .size:           8
        .value_kind:     global_buffer
      - .actual_access:  read_only
        .address_space:  global
        .offset:         48
        .size:           8
        .value_kind:     global_buffer
      - .actual_access:  read_only
        .address_space:  global
        .offset:         56
        .size:           8
        .value_kind:     global_buffer
      - .actual_access:  read_only
        .address_space:  global
        .offset:         64
        .size:           8
        .value_kind:     global_buffer
      - .actual_access:  read_only
        .address_space:  global
        .offset:         72
        .size:           8
        .value_kind:     global_buffer
      - .actual_access:  read_only
        .address_space:  global
        .offset:         80
        .size:           8
        .value_kind:     global_buffer
      - .actual_access:  read_only
        .address_space:  global
        .offset:         88
        .size:           8
        .value_kind:     global_buffer
      - .actual_access:  read_only
        .address_space:  global
        .offset:         96
        .size:           8
        .value_kind:     global_buffer
      - .actual_access:  write_only
        .address_space:  global
        .offset:         104
        .size:           8
        .value_kind:     global_buffer
    .group_segment_fixed_size: 70720
    .kernarg_segment_align: 8
    .kernarg_segment_size: 112
    .language:       OpenCL C
    .language_version:
      - 2
      - 0
    .max_flat_workgroup_size: 320
    .name:           _Z7k_att2nPKDF16_S0_PKfPfS2_S2_S2_S2_S2_S2_S2_S2_S2_S3_
    .private_segment_fixed_size: 0
    .sgpr_count:     58
    .sgpr_spill_count: 0
    .symbol:         _Z7k_att2nPKDF16_S0_PKfPfS2_S2_S2_S2_S2_S2_S2_S2_S2_S3_.kd
    .uniform_work_group_size: 1
    .uses_dynamic_stack: false
    .vgpr_count:     122
    .vgpr_spill_count: 0
    .wavefront_size: 64
  - .agpr_count:     0
    .args:
      - .actual_access:  read_only
        .address_space:  global
        .offset:         0
        .size:           8
        .value_kind:     global_buffer
      - .actual_access:  read_only
        .address_space:  global
        .offset:         8
        .size:           8
        .value_kind:     global_buffer
      - .actual_access:  read_only
        .address_space:  global
        .offset:         16
        .size:           8
        .value_kind:     global_buffer
      - .actual_access:  read_only
        .address_space:  global
        .offset:         24
        .size:           8
        .value_kind:     global_buffer
      - .actual_access:  read_only
        .address_space:  global
        .offset:         32
        .size:           8
        .value_kind:     global_buffer
      - .actual_access:  read_only
        .address_space:  global
        .offset:         40
        .size:           8
        .value_kind:     global_buffer
      - .actual_access:  read_only
        .address_space:  global
        .offset:         48
        .size:           8
        .value_kind:     global_buffer
      - .actual_access:  read_only
        .address_space:  global
        .offset:         56
        .size:           8
        .value_kind:     global_buffer
      - .actual_access:  read_only
        .address_space:  global
        .offset:         64
        .size:           8
        .value_kind:     global_buffer
      - .actual_access:  write_only
        .address_space:  global
        .offset:         72
        .size:           8
        .value_kind:     global_buffer
    .group_segment_fixed_size: 704
    .kernarg_segment_align: 8
    .kernarg_segment_size: 80
    .language:       OpenCL C
    .language_version:
      - 2
      - 0
    .max_flat_workgroup_size: 64
    .name:           _Z8k_heads3PKfS0_S0_S0_S0_S0_S0_S0_S0_Pf
    .private_segment_fixed_size: 0
    .sgpr_count:     24
    .sgpr_spill_count: 0
    .symbol:         _Z8k_heads3PKfS0_S0_S0_S0_S0_S0_S0_S0_Pf.kd
    .uniform_work_group_size: 1
    .uses_dynamic_stack: false
    .vgpr_count:     121
    .vgpr_spill_count: 0
    .wavefront_size: 64
